# baseline (speedup 1.0000x reference)
_Z11pwconv_mfmaPKfPK15HIP_vector_typeIjLj4EES0_Pf:
	s_load_dwordx4 s[12:15], s[0:1], 0x0
	s_load_dwordx4 s[16:19], s[0:1], 0x10
	s_and_b32 s20, s2, 7
	s_lshr_b32 s21, s2, 3
	s_lshr_b32 s37, s20, 1
	s_and_b32 s36, s20, 1
	s_mul_i32 s36, s36, 31
	s_add_i32 s36, s36, s21
	s_lshr_b32 s21, s36, 1
	s_and_b32 s36, s36, 1
	s_lshl_b32 s37, s37, 1
	s_add_i32 s20, s37, s36
	v_lshrrev_b32_e32 v1, 6, v0
	v_and_b32_e32 v2, 63, v0
	s_nop 0
	v_readfirstlane_b32 s22, v1
	s_nop 3
	s_lshl_b32 s23, s20, 3
	s_add_i32 s23, s23, s22
	s_mul_i32 s24, s23, 0x439200
	s_mul_i32 s25, s21, 0x1f0
	s_add_u32 s24, s24, s25
	s_lshl_b32 s25, s21, 17
	s_lshl_b32 s26, s22, 13
	s_add_u32 s25, s25, s26
	s_mul_i32 s27, s20, 0x1e080
	s_mul_i32 s36, s21, 0x1f0
	s_add_u32 s27, s27, s36
	v_lshlrev_b32_e32 v4, 4, v2
	v_and_b32_e32 v12, 31, v2
	v_min_u32_e32 v12, 30, v12
	v_lshrrev_b32_e32 v13, 5, v2
	v_lshlrev_b32_e32 v3, 4, v12
	v_mul_u32_u24_e32 v14, 0x21c900, v13
	v_add_u32_e32 v3, v3, v14
	v_lshlrev_b32_e32 v15, 9, v13
	v_cmp_lt_u32_e32 vcc, 15, v12
	s_nop 1
	v_cndmask_b32_e64 v16, 0, 1, vcc
	v_lshlrev_b32_e32 v17, 2, v12
	v_mul_u32_u24_e32 v14, 62, v16
	v_sub_u32_e32 v17, v17, v14
	v_lshl_add_u32 v14, v1, 1, v16
	v_bfe_u32 v16, v17, 1, 3
	v_xor_b32_e32 v14, v14, v16
	v_lshlrev_b32_e32 v14, 4, v14
	v_lshl_add_u32 v5, v17, 11, v14
	v_add_u32_e32 v5, v5, v15
	v_cmp_lt_u32_e32 vcc, 14, v12
	s_nop 1
	v_cndmask_b32_e64 v16, 0, 1, vcc
	v_lshlrev_b32_e32 v17, 2, v12
	v_add_u32_e32 v17, 2, v17
	v_mul_u32_u24_e32 v14, 62, v16
	v_sub_u32_e32 v17, v17, v14
	v_lshl_add_u32 v14, v1, 1, v16
	v_bfe_u32 v16, v17, 1, 3
	v_xor_b32_e32 v14, v14, v16
	v_lshlrev_b32_e32 v14, 4, v14
	v_lshl_add_u32 v10, v17, 11, v14
	v_add_u32_e32 v10, v10, v15
	s_lshl_b32 s36, s22, 2
	s_add_i32 s36, s36, 0
	s_and_b32 s36, s36, 7
	s_lshl_b32 s37, s22, 14
	s_add_i32 s37, s37, 0x0
	v_xor_b32_e32 v6, s36, v2
	v_lshlrev_b32_e32 v6, 4, v6
	v_add_u32_e32 v6, s37, v6
	s_lshl_b32 s36, s22, 2
	s_add_i32 s36, s36, 1
	s_and_b32 s36, s36, 7
	s_lshl_b32 s37, s22, 14
	s_add_i32 s37, s37, 0x1000
	v_xor_b32_e32 v7, s36, v2
	v_lshlrev_b32_e32 v7, 4, v7
	v_add_u32_e32 v7, s37, v7
	s_lshl_b32 s36, s22, 2
	s_add_i32 s36, s36, 2
	s_and_b32 s36, s36, 7
	s_lshl_b32 s37, s22, 14
	s_add_i32 s37, s37, 0x2000
	v_xor_b32_e32 v8, s36, v2
	v_lshlrev_b32_e32 v8, 4, v8
	v_add_u32_e32 v8, s37, v8
	s_lshl_b32 s36, s22, 2
	s_add_i32 s36, s36, 3
	s_and_b32 s36, s36, 7
	s_lshl_b32 s37, s22, 14
	s_add_i32 s37, s37, 0x3000
	v_xor_b32_e32 v9, s36, v2
	v_lshlrev_b32_e32 v9, 4, v9
	v_add_u32_e32 v9, s37, v9
	s_lshl_b32 s36, s22, 11
	s_add_i32 s36, s36, 0x20000
	v_add_u32_e32 v254, s36, v4
	s_add_i32 s37, s22, 1
	s_min_u32 s37, s37, 7
	s_lshl_b32 s37, s37, 11
	s_add_i32 s37, s37, 0x20000
	v_add_u32_e32 v255, s37, v4
	v_lshrrev_b32_e32 v12, 5, v0
	v_lshrrev_b32_e32 v11, 1, v12
	v_mul_u32_u24_e32 v11, 0x3c10, v11
	v_and_b32_e32 v12, 1, v12
	v_mul_u32_u24_e32 v12, 0xf8, v12
	v_add_u32_e32 v11, v11, v12
	v_and_b32_e32 v12, 31, v0
	v_lshl_add_u32 v11, v12, 3, v11
	v_add_u32_e32 v11, s27, v11
	v_cmp_eq_u32_e32 vcc, 31, v12
	v_mov_b32_e32 v12, 0x7f000000
	s_nop 1
	v_cndmask_b32_e32 v11, v11, v12, vcc
	s_waitcnt lgkmcnt(0)
	s_add_u32 s4, s12, s24
	s_addc_u32 s5, s13, 0
	s_and_b32 s5, s5, 0xffff
	s_sub_u32 s6, 0x10e48000, s24
	s_mov_b32 s7, 0x20000
	s_add_u32 s8, s14, s25
	s_addc_u32 s9, s15, 0
	s_and_b32 s9, s9, 0xffff
	s_sub_u32 s10, 0x400000, s25
	s_mov_b32 s11, 0x20000
	s_mov_b32 s28, s16
	s_and_b32 s29, s17, 0xffff
	s_mov_b32 s30, 0xf0400
	s_mov_b32 s31, 0x20000
	s_mov_b32 s32, s18
	s_and_b32 s33, s19, 0xffff
	s_mov_b32 s34, 0xf04000
	s_mov_b32 s35, 0x20000
	s_mov_b32 s40, 0x0
	s_mov_b32 s41, 0x21c90
	s_mov_b32 s42, 0x43920
	s_mov_b32 s43, 0x655b0
	s_mov_b32 s44, 0x87240
	s_mov_b32 s45, 0xa8ed0
	s_mov_b32 s46, 0xcab60
	s_mov_b32 s47, 0xec7f0
	buffer_load_dwordx4 v[44:47], v3, s[4:7], s40 offen nt
	buffer_load_dwordx4 v[48:51], v3, s[4:7], s41 offen nt
	buffer_load_dwordx4 v[52:55], v3, s[4:7], s42 offen nt
	buffer_load_dwordx4 v[56:59], v3, s[4:7], s43 offen nt
	buffer_load_dwordx4 v[60:63], v3, s[4:7], s44 offen nt
	buffer_load_dwordx4 v[64:67], v3, s[4:7], s45 offen nt
	buffer_load_dwordx4 v[68:71], v3, s[4:7], s46 offen nt
	buffer_load_dwordx4 v[72:75], v3, s[4:7], s47 offen nt
	s_mov_b32 s40, 0x10e480
	s_mov_b32 s41, 0x130110
	s_mov_b32 s42, 0x151da0
	s_mov_b32 s43, 0x173a30
	s_mov_b32 s44, 0x1956c0
	s_mov_b32 s45, 0x1b7350
	s_mov_b32 s46, 0x1d8fe0
	s_mov_b32 s47, 0x1fac70
	buffer_load_dwordx4 v[76:79], v3, s[4:7], s40 offen nt
	buffer_load_dwordx4 v[80:83], v3, s[4:7], s41 offen nt
	buffer_load_dwordx4 v[84:87], v3, s[4:7], s42 offen nt
	buffer_load_dwordx4 v[88:91], v3, s[4:7], s43 offen nt
	buffer_load_dwordx4 v[92:95], v3, s[4:7], s44 offen nt
	buffer_load_dwordx4 v[96:99], v3, s[4:7], s45 offen nt
	buffer_load_dwordx4 v[100:103], v3, s[4:7], s46 offen nt
	buffer_load_dwordx4 v[104:107], v3, s[4:7], s47 offen nt
	buffer_load_dwordx2 v[252:253], v11, s[28:31], 0 offen
	s_mov_b32 s40, 0x0
	s_mov_b32 s41, 0x400
	s_mov_b32 s42, 0x800
	s_mov_b32 s43, 0xc00
	buffer_load_dwordx4 v[108:111], v4, s[8:11], s40 offen
	buffer_load_dwordx4 v[112:115], v4, s[8:11], s41 offen
	buffer_load_dwordx4 v[116:119], v4, s[8:11], s42 offen
	buffer_load_dwordx4 v[120:123], v4, s[8:11], s43 offen
	s_mov_b32 s40, 0x1000
	s_mov_b32 s41, 0x1400
	s_mov_b32 s42, 0x1800
	s_mov_b32 s43, 0x1c00
	buffer_load_dwordx4 v[124:127], v4, s[8:11], s40 offen
	buffer_load_dwordx4 v[128:131], v4, s[8:11], s41 offen
	buffer_load_dwordx4 v[132:135], v4, s[8:11], s42 offen
	buffer_load_dwordx4 v[136:139], v4, s[8:11], s43 offen
	s_mov_b32 s40, 0x10000
	s_mov_b32 s41, 0x10400
	s_mov_b32 s42, 0x10800
	s_mov_b32 s43, 0x10c00
	buffer_load_dwordx4 v[148:151], v4, s[8:11], s40 offen
	buffer_load_dwordx4 v[152:155], v4, s[8:11], s41 offen
	buffer_load_dwordx4 v[156:159], v4, s[8:11], s42 offen
	buffer_load_dwordx4 v[160:163], v4, s[8:11], s43 offen
	s_mov_b32 s40, 0x11000
	s_mov_b32 s41, 0x11400
	s_mov_b32 s42, 0x11800
	s_mov_b32 s43, 0x11c00
	buffer_load_dwordx4 v[164:167], v4, s[8:11], s40 offen
	buffer_load_dwordx4 v[168:171], v4, s[8:11], s41 offen
	buffer_load_dwordx4 v[172:175], v4, s[8:11], s42 offen
	buffer_load_dwordx4 v[176:179], v4, s[8:11], s43 offen
	s_waitcnt vmcnt(25)
	v_cvt_pkrtz_f16_f32 v12, v44, v48
	v_cvt_pkrtz_f16_f32 v13, v52, v56
	v_cvt_pkrtz_f16_f32 v14, v60, v64
	v_cvt_pkrtz_f16_f32 v15, v68, v72
	v_cvt_pkrtz_f16_f32 v16, v45, v49
	v_cvt_pkrtz_f16_f32 v17, v53, v57
	v_cvt_pkrtz_f16_f32 v18, v61, v65
	v_cvt_pkrtz_f16_f32 v19, v69, v73
	v_cvt_pkrtz_f16_f32 v20, v46, v50
	v_cvt_pkrtz_f16_f32 v21, v54, v58
	v_cvt_pkrtz_f16_f32 v22, v62, v66
	v_cvt_pkrtz_f16_f32 v23, v70, v74
	v_cvt_pkrtz_f16_f32 v24, v47, v51
	v_cvt_pkrtz_f16_f32 v25, v55, v59
	v_cvt_pkrtz_f16_f32 v26, v63, v67
	v_cvt_pkrtz_f16_f32 v27, v71, v75
	s_mov_b32 s40, 0x3c10
	s_mov_b32 s41, 0x258a0
	s_mov_b32 s42, 0x47530
	s_mov_b32 s43, 0x691c0
	s_mov_b32 s44, 0x8ae50
	s_mov_b32 s45, 0xacae0
	s_mov_b32 s46, 0xce770
	s_mov_b32 s47, 0xf0400
	buffer_load_dwordx4 v[44:47], v3, s[4:7], s40 offen nt
	buffer_load_dwordx4 v[48:51], v3, s[4:7], s41 offen nt
	buffer_load_dwordx4 v[52:55], v3, s[4:7], s42 offen nt
	buffer_load_dwordx4 v[56:59], v3, s[4:7], s43 offen nt
	buffer_load_dwordx4 v[60:63], v3, s[4:7], s44 offen nt
	buffer_load_dwordx4 v[64:67], v3, s[4:7], s45 offen nt
	buffer_load_dwordx4 v[68:71], v3, s[4:7], s46 offen nt
	buffer_load_dwordx4 v[72:75], v3, s[4:7], s47 offen nt
	ds_write_b128 v5, v[12:15] offset:0
	ds_write_b128 v5, v[16:19] offset:2048
	ds_write_b128 v10, v[20:23] offset:0
	ds_write_b128 v10, v[24:27] offset:2048
	s_waitcnt vmcnt(25)
	v_cvt_pkrtz_f16_f32 v12, v76, v80
	v_cvt_pkrtz_f16_f32 v13, v84, v88
	v_cvt_pkrtz_f16_f32 v14, v92, v96
	v_cvt_pkrtz_f16_f32 v15, v100, v104
	v_cvt_pkrtz_f16_f32 v16, v77, v81
	v_cvt_pkrtz_f16_f32 v17, v85, v89
	v_cvt_pkrtz_f16_f32 v18, v93, v97
	v_cvt_pkrtz_f16_f32 v19, v101, v105
	v_cvt_pkrtz_f16_f32 v20, v78, v82
	v_cvt_pkrtz_f16_f32 v21, v86, v90
	v_cvt_pkrtz_f16_f32 v22, v94, v98
	v_cvt_pkrtz_f16_f32 v23, v102, v106
	v_cvt_pkrtz_f16_f32 v24, v79, v83
	v_cvt_pkrtz_f16_f32 v25, v87, v91
	v_cvt_pkrtz_f16_f32 v26, v95, v99
	v_cvt_pkrtz_f16_f32 v27, v103, v107
	s_mov_b32 s40, 0x112090
	s_mov_b32 s41, 0x133d20
	s_mov_b32 s42, 0x1559b0
	s_mov_b32 s43, 0x177640
	s_mov_b32 s44, 0x1992d0
	s_mov_b32 s45, 0x1baf60
	s_mov_b32 s46, 0x1dcbf0
	s_mov_b32 s47, 0x1fe880
	buffer_load_dwordx4 v[76:79], v3, s[4:7], s40 offen nt
	buffer_load_dwordx4 v[80:83], v3, s[4:7], s41 offen nt
	buffer_load_dwordx4 v[84:87], v3, s[4:7], s42 offen nt
	buffer_load_dwordx4 v[88:91], v3, s[4:7], s43 offen nt
	buffer_load_dwordx4 v[92:95], v3, s[4:7], s44 offen nt
	buffer_load_dwordx4 v[96:99], v3, s[4:7], s45 offen nt
	buffer_load_dwordx4 v[100:103], v3, s[4:7], s46 offen nt
	buffer_load_dwordx4 v[104:107], v3, s[4:7], s47 offen nt
	ds_write_b128 v5, v[12:15] offset:256
	ds_write_b128 v5, v[16:19] offset:2304
	ds_write_b128 v10, v[20:23] offset:256
	ds_write_b128 v10, v[24:27] offset:2304
	s_waitcnt lgkmcnt(0)
	s_barrier
	s_waitcnt vmcnt(16)
	ds_write_b128 v254, v[108:111] offset:0
	ds_write_b128 v254, v[112:115] offset:1024
	ds_write_b128 v254, v[148:151] offset:16384
	ds_write_b128 v254, v[152:155] offset:17408
	s_waitcnt lgkmcnt(0)
	s_barrier
	ds_read_b128 v[140:143], v255 offset:0
	ds_read_b128 v[144:147], v255 offset:1024
	ds_read_b128 v[180:183], v255 offset:16384
	ds_read_b128 v[184:187], v255 offset:17408
	ds_read_b128 v[12:15], v6 offset:0
	ds_read_b128 v[16:19], v6 offset:2048
	ds_read_b128 v[20:23], v7 offset:0
	ds_read_b128 v[24:27], v7 offset:2048
	ds_read_b128 v[28:31], v8 offset:0
	ds_read_b128 v[32:35], v8 offset:2048
	ds_read_b128 v[36:39], v9 offset:0
	ds_read_b128 v[40:43], v9 offset:2048
	s_waitcnt lgkmcnt(7)
	v_mfma_f32_16x16x32_f16 v[188:191], v[108:111], v[12:15], 0
	v_mfma_f32_16x16x32_f16 v[220:223], v[148:151], v[12:15], 0
	s_waitcnt lgkmcnt(6)
	v_mfma_f32_16x16x32_f16 v[192:195], v[112:115], v[16:19], 0
	v_mfma_f32_16x16x32_f16 v[224:227], v[152:155], v[16:19], 0
	s_waitcnt lgkmcnt(5)
	v_mfma_f32_16x16x32_f16 v[196:199], v[116:119], v[20:23], 0
	v_mfma_f32_16x16x32_f16 v[228:231], v[156:159], v[20:23], 0
	s_waitcnt lgkmcnt(4)
	v_mfma_f32_16x16x32_f16 v[200:203], v[120:123], v[24:27], 0
	v_mfma_f32_16x16x32_f16 v[232:235], v[160:163], v[24:27], 0
	s_waitcnt lgkmcnt(3)
	v_mfma_f32_16x16x32_f16 v[204:207], v[124:127], v[28:31], 0
	v_mfma_f32_16x16x32_f16 v[236:239], v[164:167], v[28:31], 0
	s_waitcnt lgkmcnt(2)
	v_mfma_f32_16x16x32_f16 v[208:211], v[128:131], v[32:35], 0
	v_mfma_f32_16x16x32_f16 v[240:243], v[168:171], v[32:35], 0
	s_waitcnt lgkmcnt(1)
	v_mfma_f32_16x16x32_f16 v[212:215], v[132:135], v[36:39], 0
	v_mfma_f32_16x16x32_f16 v[244:247], v[172:175], v[36:39], 0
	s_waitcnt lgkmcnt(0)
	v_mfma_f32_16x16x32_f16 v[216:219], v[136:139], v[40:43], 0
	v_mfma_f32_16x16x32_f16 v[248:251], v[176:179], v[40:43], 0
	s_waitcnt vmcnt(8)
	v_cvt_pkrtz_f16_f32 v12, v44, v48
	v_cvt_pkrtz_f16_f32 v13, v52, v56
	v_cvt_pkrtz_f16_f32 v14, v60, v64
	v_cvt_pkrtz_f16_f32 v15, v68, v72
	v_cvt_pkrtz_f16_f32 v16, v45, v49
	v_cvt_pkrtz_f16_f32 v17, v53, v57
	v_cvt_pkrtz_f16_f32 v18, v61, v65
	v_cvt_pkrtz_f16_f32 v19, v69, v73
	v_cvt_pkrtz_f16_f32 v20, v46, v50
	v_cvt_pkrtz_f16_f32 v21, v54, v58
	v_cvt_pkrtz_f16_f32 v22, v62, v66
	v_cvt_pkrtz_f16_f32 v23, v70, v74
	v_cvt_pkrtz_f16_f32 v24, v47, v51
	v_cvt_pkrtz_f16_f32 v25, v55, v59
	v_cvt_pkrtz_f16_f32 v26, v63, v67
	v_cvt_pkrtz_f16_f32 v27, v71, v75
	s_mov_b32 s40, 0x7820
	s_mov_b32 s41, 0x294b0
	s_mov_b32 s42, 0x4b140
	s_mov_b32 s43, 0x6cdd0
	s_mov_b32 s44, 0x8ea60
	s_mov_b32 s45, 0xb06f0
	s_mov_b32 s46, 0xd2380
	s_mov_b32 s47, 0xf4010
	buffer_load_dwordx4 v[44:47], v3, s[4:7], s40 offen nt
	buffer_load_dwordx4 v[48:51], v3, s[4:7], s41 offen nt
	buffer_load_dwordx4 v[52:55], v3, s[4:7], s42 offen nt
	buffer_load_dwordx4 v[56:59], v3, s[4:7], s43 offen nt
	buffer_load_dwordx4 v[60:63], v3, s[4:7], s44 offen nt
	buffer_load_dwordx4 v[64:67], v3, s[4:7], s45 offen nt
	buffer_load_dwordx4 v[68:71], v3, s[4:7], s46 offen nt
	buffer_load_dwordx4 v[72:75], v3, s[4:7], s47 offen nt
	ds_write_b128 v5, v[12:15] offset:1024
	ds_write_b128 v5, v[16:19] offset:3072
	ds_write_b128 v10, v[20:23] offset:1024
	ds_write_b128 v10, v[24:27] offset:3072
	s_waitcnt vmcnt(8)
	v_cvt_pkrtz_f16_f32 v12, v76, v80
	v_cvt_pkrtz_f16_f32 v13, v84, v88
	v_cvt_pkrtz_f16_f32 v14, v92, v96
	v_cvt_pkrtz_f16_f32 v15, v100, v104
	v_cvt_pkrtz_f16_f32 v16, v77, v81
	v_cvt_pkrtz_f16_f32 v17, v85, v89
	v_cvt_pkrtz_f16_f32 v18, v93, v97
	v_cvt_pkrtz_f16_f32 v19, v101, v105
	v_cvt_pkrtz_f16_f32 v20, v78, v82
	v_cvt_pkrtz_f16_f32 v21, v86, v90
	v_cvt_pkrtz_f16_f32 v22, v94, v98
	v_cvt_pkrtz_f16_f32 v23, v102, v106
	v_cvt_pkrtz_f16_f32 v24, v79, v83
	v_cvt_pkrtz_f16_f32 v25, v87, v91
	v_cvt_pkrtz_f16_f32 v26, v95, v99
	v_cvt_pkrtz_f16_f32 v27, v103, v107
	s_mov_b32 s40, 0x115ca0
	s_mov_b32 s41, 0x137930
	s_mov_b32 s42, 0x1595c0
	s_mov_b32 s43, 0x17b250
	s_mov_b32 s44, 0x19cee0
	s_mov_b32 s45, 0x1beb70
	s_mov_b32 s46, 0x1e0800
	s_mov_b32 s47, 0x202490
	buffer_load_dwordx4 v[76:79], v3, s[4:7], s40 offen nt
	buffer_load_dwordx4 v[80:83], v3, s[4:7], s41 offen nt
	buffer_load_dwordx4 v[84:87], v3, s[4:7], s42 offen nt
	buffer_load_dwordx4 v[88:91], v3, s[4:7], s43 offen nt
	buffer_load_dwordx4 v[92:95], v3, s[4:7], s44 offen nt
	buffer_load_dwordx4 v[96:99], v3, s[4:7], s45 offen nt
	buffer_load_dwordx4 v[100:103], v3, s[4:7], s46 offen nt
	buffer_load_dwordx4 v[104:107], v3, s[4:7], s47 offen nt
	ds_write_b128 v5, v[12:15] offset:1280
	ds_write_b128 v5, v[16:19] offset:3328
	ds_write_b128 v10, v[20:23] offset:1280
	ds_write_b128 v10, v[24:27] offset:3328
	s_waitcnt lgkmcnt(0)
	s_barrier
	ds_read_b128 v[12:15], v6 offset:1024
	ds_read_b128 v[16:19], v6 offset:3072
	ds_read_b128 v[20:23], v7 offset:1024
	ds_read_b128 v[24:27], v7 offset:3072
	ds_read_b128 v[28:31], v8 offset:1024
	ds_read_b128 v[32:35], v8 offset:3072
	ds_read_b128 v[36:39], v9 offset:1024
	ds_read_b128 v[40:43], v9 offset:3072
	s_waitcnt lgkmcnt(7)
	v_mfma_f32_16x16x32_f16 v[188:191], v[112:115], v[12:15], v[188:191]
	v_mfma_f32_16x16x32_f16 v[220:223], v[152:155], v[12:15], v[220:223]
	s_waitcnt lgkmcnt(6)
	v_mfma_f32_16x16x32_f16 v[192:195], v[116:119], v[16:19], v[192:195]
	v_mfma_f32_16x16x32_f16 v[224:227], v[156:159], v[16:19], v[224:227]
	s_waitcnt lgkmcnt(5)
	v_mfma_f32_16x16x32_f16 v[196:199], v[120:123], v[20:23], v[196:199]
	v_mfma_f32_16x16x32_f16 v[228:231], v[160:163], v[20:23], v[228:231]
	s_waitcnt lgkmcnt(4)
	v_mfma_f32_16x16x32_f16 v[200:203], v[124:127], v[24:27], v[200:203]
	v_mfma_f32_16x16x32_f16 v[232:235], v[164:167], v[24:27], v[232:235]
	s_waitcnt lgkmcnt(3)
	v_mfma_f32_16x16x32_f16 v[204:207], v[128:131], v[28:31], v[204:207]
	v_mfma_f32_16x16x32_f16 v[236:239], v[168:171], v[28:31], v[236:239]
	s_waitcnt lgkmcnt(2)
	v_mfma_f32_16x16x32_f16 v[208:211], v[132:135], v[32:35], v[208:211]
	v_mfma_f32_16x16x32_f16 v[240:243], v[172:175], v[32:35], v[240:243]
	s_waitcnt lgkmcnt(1)
	v_mfma_f32_16x16x32_f16 v[212:215], v[136:139], v[36:39], v[212:215]
	v_mfma_f32_16x16x32_f16 v[244:247], v[176:179], v[36:39], v[244:247]
	s_waitcnt lgkmcnt(0)
	v_mfma_f32_16x16x32_f16 v[216:219], v[140:143], v[40:43], v[216:219]
	v_mfma_f32_16x16x32_f16 v[248:251], v[180:183], v[40:43], v[248:251]
	s_waitcnt vmcnt(8)
	v_cvt_pkrtz_f16_f32 v12, v44, v48
	v_cvt_pkrtz_f16_f32 v13, v52, v56
	v_cvt_pkrtz_f16_f32 v14, v60, v64
	v_cvt_pkrtz_f16_f32 v15, v68, v72
	v_cvt_pkrtz_f16_f32 v16, v45, v49
	v_cvt_pkrtz_f16_f32 v17, v53, v57
	v_cvt_pkrtz_f16_f32 v18, v61, v65
	v_cvt_pkrtz_f16_f32 v19, v69, v73
	v_cvt_pkrtz_f16_f32 v20, v46, v50
	v_cvt_pkrtz_f16_f32 v21, v54, v58
	v_cvt_pkrtz_f16_f32 v22, v62, v66
	v_cvt_pkrtz_f16_f32 v23, v70, v74
	v_cvt_pkrtz_f16_f32 v24, v47, v51
	v_cvt_pkrtz_f16_f32 v25, v55, v59
	v_cvt_pkrtz_f16_f32 v26, v63, v67
	v_cvt_pkrtz_f16_f32 v27, v71, v75
	s_mov_b32 s40, 0xb430
	s_mov_b32 s41, 0x2d0c0
	s_mov_b32 s42, 0x4ed50
	s_mov_b32 s43, 0x709e0
	s_mov_b32 s44, 0x92670
	s_mov_b32 s45, 0xb4300
	s_mov_b32 s46, 0xd5f90
	s_mov_b32 s47, 0xf7c20
	buffer_load_dwordx4 v[44:47], v3, s[4:7], s40 offen nt
	buffer_load_dwordx4 v[48:51], v3, s[4:7], s41 offen nt
	buffer_load_dwordx4 v[52:55], v3, s[4:7], s42 offen nt
	buffer_load_dwordx4 v[56:59], v3, s[4:7], s43 offen nt
	buffer_load_dwordx4 v[60:63], v3, s[4:7], s44 offen nt
	buffer_load_dwordx4 v[64:67], v3, s[4:7], s45 offen nt
	buffer_load_dwordx4 v[68:71], v3, s[4:7], s46 offen nt
	buffer_load_dwordx4 v[72:75], v3, s[4:7], s47 offen nt
	ds_write_b128 v5, v[12:15] offset:0
	ds_write_b128 v5, v[16:19] offset:2048
	ds_write_b128 v10, v[20:23] offset:0
	ds_write_b128 v10, v[24:27] offset:2048
	s_waitcnt vmcnt(8)
	v_cvt_pkrtz_f16_f32 v12, v76, v80
	v_cvt_pkrtz_f16_f32 v13, v84, v88
	v_cvt_pkrtz_f16_f32 v14, v92, v96
	v_cvt_pkrtz_f16_f32 v15, v100, v104
	v_cvt_pkrtz_f16_f32 v16, v77, v81
	v_cvt_pkrtz_f16_f32 v17, v85, v89
	v_cvt_pkrtz_f16_f32 v18, v93, v97
	v_cvt_pkrtz_f16_f32 v19, v101, v105
	v_cvt_pkrtz_f16_f32 v20, v78, v82
	v_cvt_pkrtz_f16_f32 v21, v86, v90
	v_cvt_pkrtz_f16_f32 v22, v94, v98
	v_cvt_pkrtz_f16_f32 v23, v102, v106
	v_cvt_pkrtz_f16_f32 v24, v79, v83
	v_cvt_pkrtz_f16_f32 v25, v87, v91
	v_cvt_pkrtz_f16_f32 v26, v95, v99
	v_cvt_pkrtz_f16_f32 v27, v103, v107
	s_mov_b32 s40, 0x1198b0
	s_mov_b32 s41, 0x13b540
	s_mov_b32 s42, 0x15d1d0
	s_mov_b32 s43, 0x17ee60
	s_mov_b32 s44, 0x1a0af0
	s_mov_b32 s45, 0x1c2780
	s_mov_b32 s46, 0x1e4410
	s_mov_b32 s47, 0x2060a0
	buffer_load_dwordx4 v[76:79], v3, s[4:7], s40 offen nt
	buffer_load_dwordx4 v[80:83], v3, s[4:7], s41 offen nt
	buffer_load_dwordx4 v[84:87], v3, s[4:7], s42 offen nt
	buffer_load_dwordx4 v[88:91], v3, s[4:7], s43 offen nt
	buffer_load_dwordx4 v[92:95], v3, s[4:7], s44 offen nt
	buffer_load_dwordx4 v[96:99], v3, s[4:7], s45 offen nt
	buffer_load_dwordx4 v[100:103], v3, s[4:7], s46 offen nt
	buffer_load_dwordx4 v[104:107], v3, s[4:7], s47 offen nt
	ds_write_b128 v5, v[12:15] offset:256
	ds_write_b128 v5, v[16:19] offset:2304
	ds_write_b128 v10, v[20:23] offset:256
	ds_write_b128 v10, v[24:27] offset:2304
	s_waitcnt lgkmcnt(0)
	s_barrier
	ds_read_b128 v[12:15], v6 offset:0
	ds_read_b128 v[16:19], v6 offset:2048
	ds_read_b128 v[20:23], v7 offset:0
	ds_read_b128 v[24:27], v7 offset:2048
	ds_read_b128 v[28:31], v8 offset:0
	ds_read_b128 v[32:35], v8 offset:2048
	ds_read_b128 v[36:39], v9 offset:0
	ds_read_b128 v[40:43], v9 offset:2048
	s_waitcnt lgkmcnt(7)
	v_mfma_f32_16x16x32_f16 v[188:191], v[116:119], v[12:15], v[188:191]
	v_mfma_f32_16x16x32_f16 v[220:223], v[156:159], v[12:15], v[220:223]
	s_waitcnt lgkmcnt(6)
	v_mfma_f32_16x16x32_f16 v[192:195], v[120:123], v[16:19], v[192:195]
	v_mfma_f32_16x16x32_f16 v[224:227], v[160:163], v[16:19], v[224:227]
	s_waitcnt lgkmcnt(5)
	v_mfma_f32_16x16x32_f16 v[196:199], v[124:127], v[20:23], v[196:199]
	v_mfma_f32_16x16x32_f16 v[228:231], v[164:167], v[20:23], v[228:231]
	s_waitcnt lgkmcnt(4)
	v_mfma_f32_16x16x32_f16 v[200:203], v[128:131], v[24:27], v[200:203]
	v_mfma_f32_16x16x32_f16 v[232:235], v[168:171], v[24:27], v[232:235]
	s_waitcnt lgkmcnt(3)
	v_mfma_f32_16x16x32_f16 v[204:207], v[132:135], v[28:31], v[204:207]
	v_mfma_f32_16x16x32_f16 v[236:239], v[172:175], v[28:31], v[236:239]
	s_waitcnt lgkmcnt(2)
	v_mfma_f32_16x16x32_f16 v[208:211], v[136:139], v[32:35], v[208:211]
	v_mfma_f32_16x16x32_f16 v[240:243], v[176:179], v[32:35], v[240:243]
	s_waitcnt lgkmcnt(1)
	v_mfma_f32_16x16x32_f16 v[212:215], v[140:143], v[36:39], v[212:215]
	v_mfma_f32_16x16x32_f16 v[244:247], v[180:183], v[36:39], v[244:247]
	s_waitcnt lgkmcnt(0)
	v_mfma_f32_16x16x32_f16 v[216:219], v[144:147], v[40:43], v[216:219]
	v_mfma_f32_16x16x32_f16 v[248:251], v[184:187], v[40:43], v[248:251]
	s_mov_b32 s40, 0x20000
	s_mov_b32 s41, 0x20400
	s_mov_b32 s42, 0x20800
	s_mov_b32 s43, 0x20c00
	buffer_load_dwordx4 v[108:111], v4, s[8:11], s40 offen
	buffer_load_dwordx4 v[112:115], v4, s[8:11], s41 offen
	buffer_load_dwordx4 v[116:119], v4, s[8:11], s42 offen
	buffer_load_dwordx4 v[120:123], v4, s[8:11], s43 offen
	s_mov_b32 s40, 0x21000
	s_mov_b32 s41, 0x21400
	s_mov_b32 s42, 0x21800
	s_mov_b32 s43, 0x21c00
	buffer_load_dwordx4 v[124:127], v4, s[8:11], s40 offen
	buffer_load_dwordx4 v[128:131], v4, s[8:11], s41 offen
	buffer_load_dwordx4 v[132:135], v4, s[8:11], s42 offen
	buffer_load_dwordx4 v[136:139], v4, s[8:11], s43 offen
	s_waitcnt vmcnt(16)
	v_cvt_pkrtz_f16_f32 v12, v44, v48
	v_cvt_pkrtz_f16_f32 v13, v52, v56
	v_cvt_pkrtz_f16_f32 v14, v60, v64
	v_cvt_pkrtz_f16_f32 v15, v68, v72
	v_cvt_pkrtz_f16_f32 v16, v45, v49
	v_cvt_pkrtz_f16_f32 v17, v53, v57
	v_cvt_pkrtz_f16_f32 v18, v61, v65
	v_cvt_pkrtz_f16_f32 v19, v69, v73
	v_cvt_pkrtz_f16_f32 v20, v46, v50
	v_cvt_pkrtz_f16_f32 v21, v54, v58
	v_cvt_pkrtz_f16_f32 v22, v62, v66
	v_cvt_pkrtz_f16_f32 v23, v70, v74
	v_cvt_pkrtz_f16_f32 v24, v47, v51
	v_cvt_pkrtz_f16_f32 v25, v55, v59
	v_cvt_pkrtz_f16_f32 v26, v63, v67
	v_cvt_pkrtz_f16_f32 v27, v71, v75
	s_mov_b32 s40, 0xf040
	s_mov_b32 s41, 0x30cd0
	s_mov_b32 s42, 0x52960
	s_mov_b32 s43, 0x745f0
	s_mov_b32 s44, 0x96280
	s_mov_b32 s45, 0xb7f10
	s_mov_b32 s46, 0xd9ba0
	s_mov_b32 s47, 0xfb830
	buffer_load_dwordx4 v[44:47], v3, s[4:7], s40 offen nt
	buffer_load_dwordx4 v[48:51], v3, s[4:7], s41 offen nt
	buffer_load_dwordx4 v[52:55], v3, s[4:7], s42 offen nt
	buffer_load_dwordx4 v[56:59], v3, s[4:7], s43 offen nt
	buffer_load_dwordx4 v[60:63], v3, s[4:7], s44 offen nt
	buffer_load_dwordx4 v[64:67], v3, s[4:7], s45 offen nt
	buffer_load_dwordx4 v[68:71], v3, s[4:7], s46 offen nt
	buffer_load_dwordx4 v[72:75], v3, s[4:7], s47 offen nt
	ds_write_b128 v5, v[12:15] offset:1024
	ds_write_b128 v5, v[16:19] offset:3072
	ds_write_b128 v10, v[20:23] offset:1024
	ds_write_b128 v10, v[24:27] offset:3072
	s_waitcnt vmcnt(16)
	v_cvt_pkrtz_f16_f32 v12, v76, v80
	v_cvt_pkrtz_f16_f32 v13, v84, v88
	v_cvt_pkrtz_f16_f32 v14, v92, v96
	v_cvt_pkrtz_f16_f32 v15, v100, v104
	v_cvt_pkrtz_f16_f32 v16, v77, v81
	v_cvt_pkrtz_f16_f32 v17, v85, v89
	v_cvt_pkrtz_f16_f32 v18, v93, v97
	v_cvt_pkrtz_f16_f32 v19, v101, v105
	v_cvt_pkrtz_f16_f32 v20, v78, v82
	v_cvt_pkrtz_f16_f32 v21, v86, v90
	v_cvt_pkrtz_f16_f32 v22, v94, v98
	v_cvt_pkrtz_f16_f32 v23, v102, v106
	v_cvt_pkrtz_f16_f32 v24, v79, v83
	v_cvt_pkrtz_f16_f32 v25, v87, v91
	v_cvt_pkrtz_f16_f32 v26, v95, v99
	v_cvt_pkrtz_f16_f32 v27, v103, v107
	s_mov_b32 s40, 0x11d4c0
	s_mov_b32 s41, 0x13f150
	s_mov_b32 s42, 0x160de0
	s_mov_b32 s43, 0x182a70
	s_mov_b32 s44, 0x1a4700
	s_mov_b32 s45, 0x1c6390
	s_mov_b32 s46, 0x1e8020
	s_mov_b32 s47, 0x209cb0
	buffer_load_dwordx4 v[76:79], v3, s[4:7], s40 offen nt
	buffer_load_dwordx4 v[80:83], v3, s[4:7], s41 offen nt
	buffer_load_dwordx4 v[84:87], v3, s[4:7], s42 offen nt
	buffer_load_dwordx4 v[88:91], v3, s[4:7], s43 offen nt
	buffer_load_dwordx4 v[92:95], v3, s[4:7], s44 offen nt
	buffer_load_dwordx4 v[96:99], v3, s[4:7], s45 offen nt
	buffer_load_dwordx4 v[100:103], v3, s[4:7], s46 offen nt
	buffer_load_dwordx4 v[104:107], v3, s[4:7], s47 offen nt
	ds_write_b128 v5, v[12:15] offset:1280
	ds_write_b128 v5, v[16:19] offset:3328
	ds_write_b128 v10, v[20:23] offset:1280
	ds_write_b128 v10, v[24:27] offset:3328
	s_waitcnt lgkmcnt(0)
	s_barrier
	s_waitcnt vmcnt(16)
	ds_write_b128 v254, v[108:111] offset:0
	ds_write_b128 v254, v[112:115] offset:1024
	s_waitcnt lgkmcnt(0)
	s_barrier
	ds_read_b128 v[140:143], v255 offset:0
	ds_read_b128 v[144:147], v255 offset:1024
	ds_read_b128 v[12:15], v6 offset:1024
	ds_read_b128 v[16:19], v6 offset:3072
	ds_read_b128 v[20:23], v7 offset:1024
	ds_read_b128 v[24:27], v7 offset:3072
	ds_read_b128 v[28:31], v8 offset:1024
	ds_read_b128 v[32:35], v8 offset:3072
	ds_read_b128 v[36:39], v9 offset:1024
	ds_read_b128 v[40:43], v9 offset:3072
	s_waitcnt lgkmcnt(7)
	v_mfma_f32_16x16x32_f16 v[188:191], v[148:151], v[12:15], v[188:191]
	v_mfma_f32_16x16x32_f16 v[220:223], v[108:111], v[12:15], v[220:223]
	s_waitcnt lgkmcnt(6)
	v_mfma_f32_16x16x32_f16 v[192:195], v[152:155], v[16:19], v[192:195]
	v_mfma_f32_16x16x32_f16 v[224:227], v[112:115], v[16:19], v[224:227]
	s_waitcnt lgkmcnt(5)
	v_mfma_f32_16x16x32_f16 v[196:199], v[156:159], v[20:23], v[196:199]
	v_mfma_f32_16x16x32_f16 v[228:231], v[116:119], v[20:23], v[228:231]
	s_waitcnt lgkmcnt(4)
	v_mfma_f32_16x16x32_f16 v[200:203], v[160:163], v[24:27], v[200:203]
	v_mfma_f32_16x16x32_f16 v[232:235], v[120:123], v[24:27], v[232:235]
	s_waitcnt lgkmcnt(3)
	v_mfma_f32_16x16x32_f16 v[204:207], v[164:167], v[28:31], v[204:207]
	v_mfma_f32_16x16x32_f16 v[236:239], v[124:127], v[28:31], v[236:239]
	s_waitcnt lgkmcnt(2)
	v_mfma_f32_16x16x32_f16 v[208:211], v[168:171], v[32:35], v[208:211]
	v_mfma_f32_16x16x32_f16 v[240:243], v[128:131], v[32:35], v[240:243]
	s_waitcnt lgkmcnt(1)
	v_mfma_f32_16x16x32_f16 v[212:215], v[172:175], v[36:39], v[212:215]
	v_mfma_f32_16x16x32_f16 v[244:247], v[132:135], v[36:39], v[244:247]
	s_waitcnt lgkmcnt(0)
	v_mfma_f32_16x16x32_f16 v[216:219], v[176:179], v[40:43], v[216:219]
	v_mfma_f32_16x16x32_f16 v[248:251], v[136:139], v[40:43], v[248:251]
	s_waitcnt vmcnt(8)
	v_cvt_pkrtz_f16_f32 v12, v44, v48
	v_cvt_pkrtz_f16_f32 v13, v52, v56
	v_cvt_pkrtz_f16_f32 v14, v60, v64
	v_cvt_pkrtz_f16_f32 v15, v68, v72
	v_cvt_pkrtz_f16_f32 v16, v45, v49
	v_cvt_pkrtz_f16_f32 v17, v53, v57
	v_cvt_pkrtz_f16_f32 v18, v61, v65
	v_cvt_pkrtz_f16_f32 v19, v69, v73
	v_cvt_pkrtz_f16_f32 v20, v46, v50
	v_cvt_pkrtz_f16_f32 v21, v54, v58
	v_cvt_pkrtz_f16_f32 v22, v62, v66
	v_cvt_pkrtz_f16_f32 v23, v70, v74
	v_cvt_pkrtz_f16_f32 v24, v47, v51
	v_cvt_pkrtz_f16_f32 v25, v55, v59
	v_cvt_pkrtz_f16_f32 v26, v63, v67
	v_cvt_pkrtz_f16_f32 v27, v71, v75
	s_mov_b32 s40, 0x12c50
	s_mov_b32 s41, 0x348e0
	s_mov_b32 s42, 0x56570
	s_mov_b32 s43, 0x78200
	s_mov_b32 s44, 0x99e90
	s_mov_b32 s45, 0xbbb20
	s_mov_b32 s46, 0xdd7b0
	s_mov_b32 s47, 0xff440
	buffer_load_dwordx4 v[44:47], v3, s[4:7], s40 offen nt
	buffer_load_dwordx4 v[48:51], v3, s[4:7], s41 offen nt
	buffer_load_dwordx4 v[52:55], v3, s[4:7], s42 offen nt
	buffer_load_dwordx4 v[56:59], v3, s[4:7], s43 offen nt
	buffer_load_dwordx4 v[60:63], v3, s[4:7], s44 offen nt
	buffer_load_dwordx4 v[64:67], v3, s[4:7], s45 offen nt
	buffer_load_dwordx4 v[68:71], v3, s[4:7], s46 offen nt
	buffer_load_dwordx4 v[72:75], v3, s[4:7], s47 offen nt
	ds_write_b128 v5, v[12:15] offset:0
	ds_write_b128 v5, v[16:19] offset:2048
	ds_write_b128 v10, v[20:23] offset:0
	ds_write_b128 v10, v[24:27] offset:2048
	s_waitcnt vmcnt(8)
	v_cvt_pkrtz_f16_f32 v12, v76, v80
	v_cvt_pkrtz_f16_f32 v13, v84, v88
	v_cvt_pkrtz_f16_f32 v14, v92, v96
	v_cvt_pkrtz_f16_f32 v15, v100, v104
	v_cvt_pkrtz_f16_f32 v16, v77, v81
	v_cvt_pkrtz_f16_f32 v17, v85, v89
	v_cvt_pkrtz_f16_f32 v18, v93, v97
	v_cvt_pkrtz_f16_f32 v19, v101, v105
	v_cvt_pkrtz_f16_f32 v20, v78, v82
	v_cvt_pkrtz_f16_f32 v21, v86, v90
	v_cvt_pkrtz_f16_f32 v22, v94, v98
	v_cvt_pkrtz_f16_f32 v23, v102, v106
	v_cvt_pkrtz_f16_f32 v24, v79, v83
	v_cvt_pkrtz_f16_f32 v25, v87, v91
	v_cvt_pkrtz_f16_f32 v26, v95, v99
	v_cvt_pkrtz_f16_f32 v27, v103, v107
	s_mov_b32 s40, 0x1210d0
	s_mov_b32 s41, 0x142d60
	s_mov_b32 s42, 0x1649f0
	s_mov_b32 s43, 0x186680
	s_mov_b32 s44, 0x1a8310
	s_mov_b32 s45, 0x1c9fa0
	s_mov_b32 s46, 0x1ebc30
	s_mov_b32 s47, 0x20d8c0
	buffer_load_dwordx4 v[76:79], v3, s[4:7], s40 offen nt
	buffer_load_dwordx4 v[80:83], v3, s[4:7], s41 offen nt
	buffer_load_dwordx4 v[84:87], v3, s[4:7], s42 offen nt
	buffer_load_dwordx4 v[88:91], v3, s[4:7], s43 offen nt
	buffer_load_dwordx4 v[92:95], v3, s[4:7], s44 offen nt
	buffer_load_dwordx4 v[96:99], v3, s[4:7], s45 offen nt
	buffer_load_dwordx4 v[100:103], v3, s[4:7], s46 offen nt
	buffer_load_dwordx4 v[104:107], v3, s[4:7], s47 offen nt
	ds_write_b128 v5, v[12:15] offset:256
	ds_write_b128 v5, v[16:19] offset:2304
	ds_write_b128 v10, v[20:23] offset:256
	ds_write_b128 v10, v[24:27] offset:2304
	s_waitcnt lgkmcnt(0)
	s_barrier
	ds_read_b128 v[12:15], v6 offset:0
	ds_read_b128 v[16:19], v6 offset:2048
	ds_read_b128 v[20:23], v7 offset:0
	ds_read_b128 v[24:27], v7 offset:2048
	ds_read_b128 v[28:31], v8 offset:0
	ds_read_b128 v[32:35], v8 offset:2048
	ds_read_b128 v[36:39], v9 offset:0
	ds_read_b128 v[40:43], v9 offset:2048
	s_waitcnt lgkmcnt(7)
	v_mfma_f32_16x16x32_f16 v[188:191], v[152:155], v[12:15], v[188:191]
	v_mfma_f32_16x16x32_f16 v[220:223], v[112:115], v[12:15], v[220:223]
	s_waitcnt lgkmcnt(6)
	v_mfma_f32_16x16x32_f16 v[192:195], v[156:159], v[16:19], v[192:195]
	v_mfma_f32_16x16x32_f16 v[224:227], v[116:119], v[16:19], v[224:227]
	s_waitcnt lgkmcnt(5)
	v_mfma_f32_16x16x32_f16 v[196:199], v[160:163], v[20:23], v[196:199]
	v_mfma_f32_16x16x32_f16 v[228:231], v[120:123], v[20:23], v[228:231]
	s_waitcnt lgkmcnt(4)
	v_mfma_f32_16x16x32_f16 v[200:203], v[164:167], v[24:27], v[200:203]
	v_mfma_f32_16x16x32_f16 v[232:235], v[124:127], v[24:27], v[232:235]
	s_waitcnt lgkmcnt(3)
	v_mfma_f32_16x16x32_f16 v[204:207], v[168:171], v[28:31], v[204:207]
	v_mfma_f32_16x16x32_f16 v[236:239], v[128:131], v[28:31], v[236:239]
	s_waitcnt lgkmcnt(2)
	v_mfma_f32_16x16x32_f16 v[208:211], v[172:175], v[32:35], v[208:211]
	v_mfma_f32_16x16x32_f16 v[240:243], v[132:135], v[32:35], v[240:243]
	s_waitcnt lgkmcnt(1)
	v_mfma_f32_16x16x32_f16 v[212:215], v[176:179], v[36:39], v[212:215]
	v_mfma_f32_16x16x32_f16 v[244:247], v[136:139], v[36:39], v[244:247]
	s_waitcnt lgkmcnt(0)
	v_mfma_f32_16x16x32_f16 v[216:219], v[180:183], v[40:43], v[216:219]
	v_mfma_f32_16x16x32_f16 v[248:251], v[140:143], v[40:43], v[248:251]
	s_waitcnt vmcnt(8)
	v_cvt_pkrtz_f16_f32 v12, v44, v48
	v_cvt_pkrtz_f16_f32 v13, v52, v56
	v_cvt_pkrtz_f16_f32 v14, v60, v64
	v_cvt_pkrtz_f16_f32 v15, v68, v72
	v_cvt_pkrtz_f16_f32 v16, v45, v49
	v_cvt_pkrtz_f16_f32 v17, v53, v57
	v_cvt_pkrtz_f16_f32 v18, v61, v65
	v_cvt_pkrtz_f16_f32 v19, v69, v73
	v_cvt_pkrtz_f16_f32 v20, v46, v50
	v_cvt_pkrtz_f16_f32 v21, v54, v58
	v_cvt_pkrtz_f16_f32 v22, v62, v66
	v_cvt_pkrtz_f16_f32 v23, v70, v74
	v_cvt_pkrtz_f16_f32 v24, v47, v51
	v_cvt_pkrtz_f16_f32 v25, v55, v59
	v_cvt_pkrtz_f16_f32 v26, v63, v67
	v_cvt_pkrtz_f16_f32 v27, v71, v75
	s_mov_b32 s40, 0x16860
	s_mov_b32 s41, 0x384f0
	s_mov_b32 s42, 0x5a180
	s_mov_b32 s43, 0x7be10
	s_mov_b32 s44, 0x9daa0
	s_mov_b32 s45, 0xbf730
	s_mov_b32 s46, 0xe13c0
	s_mov_b32 s47, 0x103050
	buffer_load_dwordx4 v[44:47], v3, s[4:7], s40 offen nt
	buffer_load_dwordx4 v[48:51], v3, s[4:7], s41 offen nt
	buffer_load_dwordx4 v[52:55], v3, s[4:7], s42 offen nt
	buffer_load_dwordx4 v[56:59], v3, s[4:7], s43 offen nt
	buffer_load_dwordx4 v[60:63], v3, s[4:7], s44 offen nt
	buffer_load_dwordx4 v[64:67], v3, s[4:7], s45 offen nt
	buffer_load_dwordx4 v[68:71], v3, s[4:7], s46 offen nt
	buffer_load_dwordx4 v[72:75], v3, s[4:7], s47 offen nt
	ds_write_b128 v5, v[12:15] offset:1024
	ds_write_b128 v5, v[16:19] offset:3072
	ds_write_b128 v10, v[20:23] offset:1024
	ds_write_b128 v10, v[24:27] offset:3072
	s_waitcnt vmcnt(8)
	v_cvt_pkrtz_f16_f32 v12, v76, v80
	v_cvt_pkrtz_f16_f32 v13, v84, v88
	v_cvt_pkrtz_f16_f32 v14, v92, v96
	v_cvt_pkrtz_f16_f32 v15, v100, v104
	v_cvt_pkrtz_f16_f32 v16, v77, v81
	v_cvt_pkrtz_f16_f32 v17, v85, v89
	v_cvt_pkrtz_f16_f32 v18, v93, v97
	v_cvt_pkrtz_f16_f32 v19, v101, v105
	v_cvt_pkrtz_f16_f32 v20, v78, v82
	v_cvt_pkrtz_f16_f32 v21, v86, v90
	v_cvt_pkrtz_f16_f32 v22, v94, v98
	v_cvt_pkrtz_f16_f32 v23, v102, v106
	v_cvt_pkrtz_f16_f32 v24, v79, v83
	v_cvt_pkrtz_f16_f32 v25, v87, v91
	v_cvt_pkrtz_f16_f32 v26, v95, v99
	v_cvt_pkrtz_f16_f32 v27, v103, v107
	s_mov_b32 s40, 0x124ce0
	s_mov_b32 s41, 0x146970
	s_mov_b32 s42, 0x168600
	s_mov_b32 s43, 0x18a290
	s_mov_b32 s44, 0x1abf20
	s_mov_b32 s45, 0x1cdbb0
	s_mov_b32 s46, 0x1ef840
	s_mov_b32 s47, 0x2114d0
	buffer_load_dwordx4 v[76:79], v3, s[4:7], s40 offen nt
	buffer_load_dwordx4 v[80:83], v3, s[4:7], s41 offen nt
	buffer_load_dwordx4 v[84:87], v3, s[4:7], s42 offen nt
	buffer_load_dwordx4 v[88:91], v3, s[4:7], s43 offen nt
	buffer_load_dwordx4 v[92:95], v3, s[4:7], s44 offen nt
	buffer_load_dwordx4 v[96:99], v3, s[4:7], s45 offen nt
	buffer_load_dwordx4 v[100:103], v3, s[4:7], s46 offen nt
	buffer_load_dwordx4 v[104:107], v3, s[4:7], s47 offen nt
	ds_write_b128 v5, v[12:15] offset:1280
	ds_write_b128 v5, v[16:19] offset:3328
	ds_write_b128 v10, v[20:23] offset:1280
	ds_write_b128 v10, v[24:27] offset:3328
	s_waitcnt lgkmcnt(0)
	s_barrier
	ds_read_b128 v[12:15], v6 offset:1024
	ds_read_b128 v[16:19], v6 offset:3072
	ds_read_b128 v[20:23], v7 offset:1024
	ds_read_b128 v[24:27], v7 offset:3072
	ds_read_b128 v[28:31], v8 offset:1024
	ds_read_b128 v[32:35], v8 offset:3072
	ds_read_b128 v[36:39], v9 offset:1024
	ds_read_b128 v[40:43], v9 offset:3072
	s_waitcnt lgkmcnt(7)
	v_mfma_f32_16x16x32_f16 v[188:191], v[156:159], v[12:15], v[188:191]
	v_mfma_f32_16x16x32_f16 v[220:223], v[116:119], v[12:15], v[220:223]
	s_waitcnt lgkmcnt(6)
	v_mfma_f32_16x16x32_f16 v[192:195], v[160:163], v[16:19], v[192:195]
	v_mfma_f32_16x16x32_f16 v[224:227], v[120:123], v[16:19], v[224:227]
	s_waitcnt lgkmcnt(5)
	v_mfma_f32_16x16x32_f16 v[196:199], v[164:167], v[20:23], v[196:199]
	v_mfma_f32_16x16x32_f16 v[228:231], v[124:127], v[20:23], v[228:231]
	s_waitcnt lgkmcnt(4)
	v_mfma_f32_16x16x32_f16 v[200:203], v[168:171], v[24:27], v[200:203]
	v_mfma_f32_16x16x32_f16 v[232:235], v[128:131], v[24:27], v[232:235]
	s_waitcnt lgkmcnt(3)
	v_mfma_f32_16x16x32_f16 v[204:207], v[172:175], v[28:31], v[204:207]
	v_mfma_f32_16x16x32_f16 v[236:239], v[132:135], v[28:31], v[236:239]
	s_waitcnt lgkmcnt(2)
	v_mfma_f32_16x16x32_f16 v[208:211], v[176:179], v[32:35], v[208:211]
	v_mfma_f32_16x16x32_f16 v[240:243], v[136:139], v[32:35], v[240:243]
	s_waitcnt lgkmcnt(1)
	v_mfma_f32_16x16x32_f16 v[212:215], v[180:183], v[36:39], v[212:215]
	v_mfma_f32_16x16x32_f16 v[244:247], v[140:143], v[36:39], v[244:247]
	s_waitcnt lgkmcnt(0)
	v_mfma_f32_16x16x32_f16 v[216:219], v[184:187], v[40:43], v[216:219]
	v_mfma_f32_16x16x32_f16 v[248:251], v[144:147], v[40:43], v[248:251]
	s_mov_b32 s40, 0x30000
	s_mov_b32 s41, 0x30400
	s_mov_b32 s42, 0x30800
	s_mov_b32 s43, 0x30c00
	buffer_load_dwordx4 v[148:151], v4, s[8:11], s40 offen
	buffer_load_dwordx4 v[152:155], v4, s[8:11], s41 offen
	buffer_load_dwordx4 v[156:159], v4, s[8:11], s42 offen
	buffer_load_dwordx4 v[160:163], v4, s[8:11], s43 offen
	s_mov_b32 s40, 0x31000
	s_mov_b32 s41, 0x31400
	s_mov_b32 s42, 0x31800
	s_mov_b32 s43, 0x31c00
	buffer_load_dwordx4 v[164:167], v4, s[8:11], s40 offen
	buffer_load_dwordx4 v[168:171], v4, s[8:11], s41 offen
	buffer_load_dwordx4 v[172:175], v4, s[8:11], s42 offen
	buffer_load_dwordx4 v[176:179], v4, s[8:11], s43 offen
	s_waitcnt vmcnt(16)
	v_cvt_pkrtz_f16_f32 v12, v44, v48
	v_cvt_pkrtz_f16_f32 v13, v52, v56
	v_cvt_pkrtz_f16_f32 v14, v60, v64
	v_cvt_pkrtz_f16_f32 v15, v68, v72
	v_cvt_pkrtz_f16_f32 v16, v45, v49
	v_cvt_pkrtz_f16_f32 v17, v53, v57
	v_cvt_pkrtz_f16_f32 v18, v61, v65
	v_cvt_pkrtz_f16_f32 v19, v69, v73
	v_cvt_pkrtz_f16_f32 v20, v46, v50
	v_cvt_pkrtz_f16_f32 v21, v54, v58
	v_cvt_pkrtz_f16_f32 v22, v62, v66
	v_cvt_pkrtz_f16_f32 v23, v70, v74
	v_cvt_pkrtz_f16_f32 v24, v47, v51
	v_cvt_pkrtz_f16_f32 v25, v55, v59
	v_cvt_pkrtz_f16_f32 v26, v63, v67
	v_cvt_pkrtz_f16_f32 v27, v71, v75
	s_mov_b32 s40, 0x1a470
	s_mov_b32 s41, 0x3c100
	s_mov_b32 s42, 0x5dd90
	s_mov_b32 s43, 0x7fa20
	s_mov_b32 s44, 0xa16b0
	s_mov_b32 s45, 0xc3340
	s_mov_b32 s46, 0xe4fd0
	s_mov_b32 s47, 0x106c60
	buffer_load_dwordx4 v[44:47], v3, s[4:7], s40 offen nt
	buffer_load_dwordx4 v[48:51], v3, s[4:7], s41 offen nt
	buffer_load_dwordx4 v[52:55], v3, s[4:7], s42 offen nt
	buffer_load_dwordx4 v[56:59], v3, s[4:7], s43 offen nt
	buffer_load_dwordx4 v[60:63], v3, s[4:7], s44 offen nt
	buffer_load_dwordx4 v[64:67], v3, s[4:7], s45 offen nt
	buffer_load_dwordx4 v[68:71], v3, s[4:7], s46 offen nt
	buffer_load_dwordx4 v[72:75], v3, s[4:7], s47 offen nt
	ds_write_b128 v5, v[12:15] offset:0
	ds_write_b128 v5, v[16:19] offset:2048
	ds_write_b128 v10, v[20:23] offset:0
	ds_write_b128 v10, v[24:27] offset:2048
	s_waitcnt vmcnt(16)
	v_cvt_pkrtz_f16_f32 v12, v76, v80
	v_cvt_pkrtz_f16_f32 v13, v84, v88
	v_cvt_pkrtz_f16_f32 v14, v92, v96
	v_cvt_pkrtz_f16_f32 v15, v100, v104
	v_cvt_pkrtz_f16_f32 v16, v77, v81
	v_cvt_pkrtz_f16_f32 v17, v85, v89
	v_cvt_pkrtz_f16_f32 v18, v93, v97
	v_cvt_pkrtz_f16_f32 v19, v101, v105
	v_cvt_pkrtz_f16_f32 v20, v78, v82
	v_cvt_pkrtz_f16_f32 v21, v86, v90
	v_cvt_pkrtz_f16_f32 v22, v94, v98
	v_cvt_pkrtz_f16_f32 v23, v102, v106
	v_cvt_pkrtz_f16_f32 v24, v79, v83
	v_cvt_pkrtz_f16_f32 v25, v87, v91
	v_cvt_pkrtz_f16_f32 v26, v95, v99
	v_cvt_pkrtz_f16_f32 v27, v103, v107
	s_mov_b32 s40, 0x1288f0
	s_mov_b32 s41, 0x14a580
	s_mov_b32 s42, 0x16c210
	s_mov_b32 s43, 0x18dea0
	s_mov_b32 s44, 0x1afb30
	s_mov_b32 s45, 0x1d17c0
	s_mov_b32 s46, 0x1f3450
	s_mov_b32 s47, 0x2150e0
	buffer_load_dwordx4 v[76:79], v3, s[4:7], s40 offen nt
	buffer_load_dwordx4 v[80:83], v3, s[4:7], s41 offen nt
	buffer_load_dwordx4 v[84:87], v3, s[4:7], s42 offen nt
	buffer_load_dwordx4 v[88:91], v3, s[4:7], s43 offen nt
	buffer_load_dwordx4 v[92:95], v3, s[4:7], s44 offen nt
	buffer_load_dwordx4 v[96:99], v3, s[4:7], s45 offen nt
	buffer_load_dwordx4 v[100:103], v3, s[4:7], s46 offen nt
	buffer_load_dwordx4 v[104:107], v3, s[4:7], s47 offen nt
	ds_write_b128 v5, v[12:15] offset:256
	ds_write_b128 v5, v[16:19] offset:2304
	ds_write_b128 v10, v[20:23] offset:256
	ds_write_b128 v10, v[24:27] offset:2304
	s_waitcnt lgkmcnt(0)
	s_barrier
	s_waitcnt vmcnt(16)
	ds_write_b128 v254, v[148:151] offset:16384
	ds_write_b128 v254, v[152:155] offset:17408
	s_waitcnt lgkmcnt(0)
	s_barrier
	ds_read_b128 v[180:183], v255 offset:16384
	ds_read_b128 v[184:187], v255 offset:17408
	ds_read_b128 v[12:15], v6 offset:0
	ds_read_b128 v[16:19], v6 offset:2048
	ds_read_b128 v[20:23], v7 offset:0
	ds_read_b128 v[24:27], v7 offset:2048
	ds_read_b128 v[28:31], v8 offset:0
	ds_read_b128 v[32:35], v8 offset:2048
	ds_read_b128 v[36:39], v9 offset:0
	ds_read_b128 v[40:43], v9 offset:2048
	s_waitcnt lgkmcnt(7)
	v_mfma_f32_16x16x32_f16 v[188:191], v[108:111], v[12:15], v[188:191]
	v_mfma_f32_16x16x32_f16 v[220:223], v[148:151], v[12:15], v[220:223]
	s_waitcnt lgkmcnt(6)
	v_mfma_f32_16x16x32_f16 v[192:195], v[112:115], v[16:19], v[192:195]
	v_mfma_f32_16x16x32_f16 v[224:227], v[152:155], v[16:19], v[224:227]
	s_waitcnt lgkmcnt(5)
	v_mfma_f32_16x16x32_f16 v[196:199], v[116:119], v[20:23], v[196:199]
	v_mfma_f32_16x16x32_f16 v[228:231], v[156:159], v[20:23], v[228:231]
	s_waitcnt lgkmcnt(4)
	v_mfma_f32_16x16x32_f16 v[200:203], v[120:123], v[24:27], v[200:203]
	v_mfma_f32_16x16x32_f16 v[232:235], v[160:163], v[24:27], v[232:235]
	s_waitcnt lgkmcnt(3)
	v_mfma_f32_16x16x32_f16 v[204:207], v[124:127], v[28:31], v[204:207]
	v_mfma_f32_16x16x32_f16 v[236:239], v[164:167], v[28:31], v[236:239]
	s_waitcnt lgkmcnt(2)
	v_mfma_f32_16x16x32_f16 v[208:211], v[128:131], v[32:35], v[208:211]
	v_mfma_f32_16x16x32_f16 v[240:243], v[168:171], v[32:35], v[240:243]
	s_waitcnt lgkmcnt(1)
	v_mfma_f32_16x16x32_f16 v[212:215], v[132:135], v[36:39], v[212:215]
	v_mfma_f32_16x16x32_f16 v[244:247], v[172:175], v[36:39], v[244:247]
	s_waitcnt lgkmcnt(0)
	v_mfma_f32_16x16x32_f16 v[216:219], v[136:139], v[40:43], v[216:219]
	v_mfma_f32_16x16x32_f16 v[248:251], v[176:179], v[40:43], v[248:251]
	s_waitcnt vmcnt(8)
	v_cvt_pkrtz_f16_f32 v12, v44, v48
	v_cvt_pkrtz_f16_f32 v13, v52, v56
	v_cvt_pkrtz_f16_f32 v14, v60, v64
	v_cvt_pkrtz_f16_f32 v15, v68, v72
	v_cvt_pkrtz_f16_f32 v16, v45, v49
	v_cvt_pkrtz_f16_f32 v17, v53, v57
	v_cvt_pkrtz_f16_f32 v18, v61, v65
	v_cvt_pkrtz_f16_f32 v19, v69, v73
	v_cvt_pkrtz_f16_f32 v20, v46, v50
	v_cvt_pkrtz_f16_f32 v21, v54, v58
	v_cvt_pkrtz_f16_f32 v22, v62, v66
	v_cvt_pkrtz_f16_f32 v23, v70, v74
	v_cvt_pkrtz_f16_f32 v24, v47, v51
	v_cvt_pkrtz_f16_f32 v25, v55, v59
	v_cvt_pkrtz_f16_f32 v26, v63, v67
	v_cvt_pkrtz_f16_f32 v27, v71, v75
	s_mov_b32 s40, 0x1e080
	s_mov_b32 s41, 0x3fd10
	s_mov_b32 s42, 0x619a0
	s_mov_b32 s43, 0x83630
	s_mov_b32 s44, 0xa52c0
	s_mov_b32 s45, 0xc6f50
	s_mov_b32 s46, 0xe8be0
	s_mov_b32 s47, 0x10a870
	buffer_load_dwordx4 v[44:47], v3, s[4:7], s40 offen nt
	buffer_load_dwordx4 v[48:51], v3, s[4:7], s41 offen nt
	buffer_load_dwordx4 v[52:55], v3, s[4:7], s42 offen nt
	buffer_load_dwordx4 v[56:59], v3, s[4:7], s43 offen nt
	buffer_load_dwordx4 v[60:63], v3, s[4:7], s44 offen nt
	buffer_load_dwordx4 v[64:67], v3, s[4:7], s45 offen nt
	buffer_load_dwordx4 v[68:71], v3, s[4:7], s46 offen nt
	buffer_load_dwordx4 v[72:75], v3, s[4:7], s47 offen nt
	ds_write_b128 v5, v[12:15] offset:1024
	ds_write_b128 v5, v[16:19] offset:3072
	ds_write_b128 v10, v[20:23] offset:1024
	ds_write_b128 v10, v[24:27] offset:3072
	s_waitcnt vmcnt(8)
	v_cvt_pkrtz_f16_f32 v12, v76, v80
	v_cvt_pkrtz_f16_f32 v13, v84, v88
	v_cvt_pkrtz_f16_f32 v14, v92, v96
	v_cvt_pkrtz_f16_f32 v15, v100, v104
	v_cvt_pkrtz_f16_f32 v16, v77, v81
	v_cvt_pkrtz_f16_f32 v17, v85, v89
	v_cvt_pkrtz_f16_f32 v18, v93, v97
	v_cvt_pkrtz_f16_f32 v19, v101, v105
	v_cvt_pkrtz_f16_f32 v20, v78, v82
	v_cvt_pkrtz_f16_f32 v21, v86, v90
	v_cvt_pkrtz_f16_f32 v22, v94, v98
	v_cvt_pkrtz_f16_f32 v23, v102, v106
	v_cvt_pkrtz_f16_f32 v24, v79, v83
	v_cvt_pkrtz_f16_f32 v25, v87, v91
	v_cvt_pkrtz_f16_f32 v26, v95, v99
	v_cvt_pkrtz_f16_f32 v27, v103, v107
	s_mov_b32 s40, 0x12c500
	s_mov_b32 s41, 0x14e190
	s_mov_b32 s42, 0x16fe20
	s_mov_b32 s43, 0x191ab0
	s_mov_b32 s44, 0x1b3740
	s_mov_b32 s45, 0x1d53d0
	s_mov_b32 s46, 0x1f7060
	s_mov_b32 s47, 0x218cf0
	buffer_load_dwordx4 v[76:79], v3, s[4:7], s40 offen nt
	buffer_load_dwordx4 v[80:83], v3, s[4:7], s41 offen nt
	buffer_load_dwordx4 v[84:87], v3, s[4:7], s42 offen nt
	buffer_load_dwordx4 v[88:91], v3, s[4:7], s43 offen nt
	buffer_load_dwordx4 v[92:95], v3, s[4:7], s44 offen nt
	buffer_load_dwordx4 v[96:99], v3, s[4:7], s45 offen nt
	buffer_load_dwordx4 v[100:103], v3, s[4:7], s46 offen nt
	buffer_load_dwordx4 v[104:107], v3, s[4:7], s47 offen nt
	ds_write_b128 v5, v[12:15] offset:1280
	ds_write_b128 v5, v[16:19] offset:3328
	ds_write_b128 v10, v[20:23] offset:1280
	ds_write_b128 v10, v[24:27] offset:3328
	s_waitcnt lgkmcnt(0)
	s_barrier
	ds_read_b128 v[12:15], v6 offset:1024
	ds_read_b128 v[16:19], v6 offset:3072
	ds_read_b128 v[20:23], v7 offset:1024
	ds_read_b128 v[24:27], v7 offset:3072
	ds_read_b128 v[28:31], v8 offset:1024
	ds_read_b128 v[32:35], v8 offset:3072
	ds_read_b128 v[36:39], v9 offset:1024
	ds_read_b128 v[40:43], v9 offset:3072
	s_waitcnt lgkmcnt(7)
	v_mfma_f32_16x16x32_f16 v[188:191], v[112:115], v[12:15], v[188:191]
	v_mfma_f32_16x16x32_f16 v[220:223], v[152:155], v[12:15], v[220:223]
	s_waitcnt lgkmcnt(6)
	v_mfma_f32_16x16x32_f16 v[192:195], v[116:119], v[16:19], v[192:195]
	v_mfma_f32_16x16x32_f16 v[224:227], v[156:159], v[16:19], v[224:227]
	s_waitcnt lgkmcnt(5)
	v_mfma_f32_16x16x32_f16 v[196:199], v[120:123], v[20:23], v[196:199]
	v_mfma_f32_16x16x32_f16 v[228:231], v[160:163], v[20:23], v[228:231]
	s_waitcnt lgkmcnt(4)
	v_mfma_f32_16x16x32_f16 v[200:203], v[124:127], v[24:27], v[200:203]
	v_mfma_f32_16x16x32_f16 v[232:235], v[164:167], v[24:27], v[232:235]
	s_waitcnt lgkmcnt(3)
	v_mfma_f32_16x16x32_f16 v[204:207], v[128:131], v[28:31], v[204:207]
	v_mfma_f32_16x16x32_f16 v[236:239], v[168:171], v[28:31], v[236:239]
	s_waitcnt lgkmcnt(2)
	v_mfma_f32_16x16x32_f16 v[208:211], v[132:135], v[32:35], v[208:211]
	v_mfma_f32_16x16x32_f16 v[240:243], v[172:175], v[32:35], v[240:243]
	s_waitcnt lgkmcnt(1)
	v_mfma_f32_16x16x32_f16 v[212:215], v[136:139], v[36:39], v[212:215]
	v_mfma_f32_16x16x32_f16 v[244:247], v[176:179], v[36:39], v[244:247]
	s_waitcnt lgkmcnt(0)
	v_mfma_f32_16x16x32_f16 v[216:219], v[140:143], v[40:43], v[216:219]
	v_mfma_f32_16x16x32_f16 v[248:251], v[180:183], v[40:43], v[248:251]
	s_waitcnt vmcnt(8)
	v_cvt_pkrtz_f16_f32 v12, v44, v48
	v_cvt_pkrtz_f16_f32 v13, v52, v56
	v_cvt_pkrtz_f16_f32 v14, v60, v64
	v_cvt_pkrtz_f16_f32 v15, v68, v72
	v_cvt_pkrtz_f16_f32 v16, v45, v49
	v_cvt_pkrtz_f16_f32 v17, v53, v57
	v_cvt_pkrtz_f16_f32 v18, v61, v65
	v_cvt_pkrtz_f16_f32 v19, v69, v73
	v_cvt_pkrtz_f16_f32 v20, v46, v50
	v_cvt_pkrtz_f16_f32 v21, v54, v58
	v_cvt_pkrtz_f16_f32 v22, v62, v66
	v_cvt_pkrtz_f16_f32 v23, v70, v74
	v_cvt_pkrtz_f16_f32 v24, v47, v51
	v_cvt_pkrtz_f16_f32 v25, v55, v59
	v_cvt_pkrtz_f16_f32 v26, v63, v67
	v_cvt_pkrtz_f16_f32 v27, v71, v75
	ds_write_b128 v5, v[12:15] offset:0
	ds_write_b128 v5, v[16:19] offset:2048
	ds_write_b128 v10, v[20:23] offset:0
	ds_write_b128 v10, v[24:27] offset:2048
	s_waitcnt vmcnt(0)
	v_cvt_pkrtz_f16_f32 v12, v76, v80
	v_cvt_pkrtz_f16_f32 v13, v84, v88
	v_cvt_pkrtz_f16_f32 v14, v92, v96
	v_cvt_pkrtz_f16_f32 v15, v100, v104
	v_cvt_pkrtz_f16_f32 v16, v77, v81
	v_cvt_pkrtz_f16_f32 v17, v85, v89
	v_cvt_pkrtz_f16_f32 v18, v93, v97
	v_cvt_pkrtz_f16_f32 v19, v101, v105
	v_cvt_pkrtz_f16_f32 v20, v78, v82
	v_cvt_pkrtz_f16_f32 v21, v86, v90
	v_cvt_pkrtz_f16_f32 v22, v94, v98
	v_cvt_pkrtz_f16_f32 v23, v102, v106
	v_cvt_pkrtz_f16_f32 v24, v79, v83
	v_cvt_pkrtz_f16_f32 v25, v87, v91
	v_cvt_pkrtz_f16_f32 v26, v95, v99
	v_cvt_pkrtz_f16_f32 v27, v103, v107
	ds_write_b128 v5, v[12:15] offset:256
	ds_write_b128 v5, v[16:19] offset:2304
	ds_write_b128 v10, v[20:23] offset:256
	ds_write_b128 v10, v[24:27] offset:2304
	s_waitcnt lgkmcnt(0)
	s_barrier
	ds_read_b128 v[12:15], v6 offset:0
	ds_read_b128 v[16:19], v6 offset:2048
	ds_read_b128 v[20:23], v7 offset:0
	ds_read_b128 v[24:27], v7 offset:2048
	ds_read_b128 v[28:31], v8 offset:0
	ds_read_b128 v[32:35], v8 offset:2048
	ds_read_b128 v[36:39], v9 offset:0
	ds_read_b128 v[40:43], v9 offset:2048
	s_waitcnt lgkmcnt(7)
	v_mfma_f32_16x16x32_f16 v[188:191], v[116:119], v[12:15], v[188:191]
	v_mfma_f32_16x16x32_f16 v[220:223], v[156:159], v[12:15], v[220:223]
	s_waitcnt lgkmcnt(6)
	v_mfma_f32_16x16x32_f16 v[192:195], v[120:123], v[16:19], v[192:195]
	v_mfma_f32_16x16x32_f16 v[224:227], v[160:163], v[16:19], v[224:227]
	s_waitcnt lgkmcnt(5)
	v_mfma_f32_16x16x32_f16 v[196:199], v[124:127], v[20:23], v[196:199]
	v_mfma_f32_16x16x32_f16 v[228:231], v[164:167], v[20:23], v[228:231]
	s_waitcnt lgkmcnt(4)
	v_mfma_f32_16x16x32_f16 v[200:203], v[128:131], v[24:27], v[200:203]
	v_mfma_f32_16x16x32_f16 v[232:235], v[168:171], v[24:27], v[232:235]
	s_waitcnt lgkmcnt(3)
	v_mfma_f32_16x16x32_f16 v[204:207], v[132:135], v[28:31], v[204:207]
	v_mfma_f32_16x16x32_f16 v[236:239], v[172:175], v[28:31], v[236:239]
	s_waitcnt lgkmcnt(2)
	v_mfma_f32_16x16x32_f16 v[208:211], v[136:139], v[32:35], v[208:211]
	v_mfma_f32_16x16x32_f16 v[240:243], v[176:179], v[32:35], v[240:243]
	s_waitcnt lgkmcnt(1)
	v_mfma_f32_16x16x32_f16 v[212:215], v[140:143], v[36:39], v[212:215]
	v_mfma_f32_16x16x32_f16 v[244:247], v[180:183], v[36:39], v[244:247]
	s_waitcnt lgkmcnt(0)
	v_mfma_f32_16x16x32_f16 v[216:219], v[144:147], v[40:43], v[216:219]
	v_mfma_f32_16x16x32_f16 v[248:251], v[184:187], v[40:43], v[248:251]
	s_nop 7
	s_nop 3
	v_and_b32_e32 v44, 1, v0
	v_cmp_eq_u32_e32 vcc, 1, v44
	s_nop 1
	v_cndmask_b32_e32 v188, v188, v220, vcc
	v_cndmask_b32_e32 v189, v189, v221, vcc
	v_cndmask_b32_e32 v190, v190, v222, vcc
	v_cndmask_b32_e32 v191, v191, v223, vcc
	v_cndmask_b32_e32 v192, v192, v224, vcc
	v_cndmask_b32_e32 v193, v193, v225, vcc
	v_cndmask_b32_e32 v194, v194, v226, vcc
	v_cndmask_b32_e32 v195, v195, v227, vcc
	v_cndmask_b32_e32 v196, v196, v228, vcc
	v_cndmask_b32_e32 v197, v197, v229, vcc
	v_cndmask_b32_e32 v198, v198, v230, vcc
	v_cndmask_b32_e32 v199, v199, v231, vcc
	v_cndmask_b32_e32 v200, v200, v232, vcc
	v_cndmask_b32_e32 v201, v201, v233, vcc
	v_cndmask_b32_e32 v202, v202, v234, vcc
	v_cndmask_b32_e32 v203, v203, v235, vcc
	v_cndmask_b32_e32 v204, v204, v236, vcc
	v_cndmask_b32_e32 v205, v205, v237, vcc
	v_cndmask_b32_e32 v206, v206, v238, vcc
	v_cndmask_b32_e32 v207, v207, v239, vcc
	v_cndmask_b32_e32 v208, v208, v240, vcc
	v_cndmask_b32_e32 v209, v209, v241, vcc
	v_cndmask_b32_e32 v210, v210, v242, vcc
	v_cndmask_b32_e32 v211, v211, v243, vcc
	v_cndmask_b32_e32 v212, v212, v244, vcc
	v_cndmask_b32_e32 v213, v213, v245, vcc
	v_cndmask_b32_e32 v214, v214, v246, vcc
	v_cndmask_b32_e32 v215, v215, v247, vcc
	v_cndmask_b32_e32 v216, v216, v248, vcc
	v_cndmask_b32_e32 v217, v217, v249, vcc
	v_cndmask_b32_e32 v218, v218, v250, vcc
	v_cndmask_b32_e32 v219, v219, v251, vcc
	s_barrier
	v_lshrrev_b32_e32 v44, 4, v2
	v_lshlrev_b32_e32 v44, 6, v44
	v_and_b32_e32 v12, 15, v2
	v_add_u32_e32 v44, v44, v12
	v_mul_u32_u24_e32 v44, 0x108, v44
	v_lshl_add_u32 v44, v1, 5, v44
	ds_write_b32 v44, v188 offset:0
	ds_write_b32 v44, v189 offset:4224
	ds_write_b32 v44, v190 offset:8448
	ds_write_b32 v44, v191 offset:12672
	ds_write_b32 v44, v192 offset:4
	ds_write_b32 v44, v193 offset:4228
	ds_write_b32 v44, v194 offset:8452
	ds_write_b32 v44, v195 offset:12676
	s_waitcnt lgkmcnt(4)
	ds_write_b32 v44, v196 offset:8
	ds_write_b32 v44, v197 offset:4232
	ds_write_b32 v44, v198 offset:8456
	ds_write_b32 v44, v199 offset:12680
	ds_write_b32 v44, v200 offset:12
	ds_write_b32 v44, v201 offset:4236
	ds_write_b32 v44, v202 offset:8460
	ds_write_b32 v44, v203 offset:12684
	s_waitcnt lgkmcnt(4)
	ds_write_b32 v44, v204 offset:16
	ds_write_b32 v44, v205 offset:4240
	ds_write_b32 v44, v206 offset:8464
	ds_write_b32 v44, v207 offset:12688
	ds_write_b32 v44, v208 offset:20
	ds_write_b32 v44, v209 offset:4244
	ds_write_b32 v44, v210 offset:8468
	ds_write_b32 v44, v211 offset:12692
	s_waitcnt lgkmcnt(4)
	ds_write_b32 v44, v212 offset:24
	ds_write_b32 v44, v213 offset:4248
	ds_write_b32 v44, v214 offset:8472
	ds_write_b32 v44, v215 offset:12696
	ds_write_b32 v44, v216 offset:28
	ds_write_b32 v44, v217 offset:4252
	ds_write_b32 v44, v218 offset:8476
	ds_write_b32 v44, v219 offset:12700
	s_waitcnt lgkmcnt(0)
	s_barrier
	v_lshrrev_b32_e32 v12, 5, v0
	v_mul_u32_u24_e32 v12, 0x108, v12
	v_and_b32_e32 v13, 31, v0
	v_lshl_add_u32 v12, v13, 3, v12
	ds_read_b64 v[44:45], v12 offset:0
	ds_read_b64 v[46:47], v12 offset:4224
	ds_read_b64 v[48:49], v12 offset:8448
	ds_read_b64 v[50:51], v12 offset:12672
	ds_read_b64 v[52:53], v12 offset:16896
	ds_read_b64 v[54:55], v12 offset:21120
	ds_read_b64 v[56:57], v12 offset:25344
	ds_read_b64 v[58:59], v12 offset:29568
	s_waitcnt lgkmcnt(7)
	v_add_f32_e32 v44, v252, v44
	v_add_f32_e32 v45, v253, v45
	s_mov_b32 s40, 0x0
	buffer_store_dwordx2 v[44:45], v11, s[32:35], s40 offen nt
	s_waitcnt lgkmcnt(6)
	v_add_f32_e32 v46, v252, v46
	v_add_f32_e32 v47, v253, v47
	s_mov_b32 s41, 0xf0400
	buffer_store_dwordx2 v[46:47], v11, s[32:35], s41 offen nt
	s_waitcnt lgkmcnt(5)
	v_add_f32_e32 v48, v252, v48
	v_add_f32_e32 v49, v253, v49
	s_mov_b32 s42, 0x1e0800
	buffer_store_dwordx2 v[48:49], v11, s[32:35], s42 offen nt
	s_waitcnt lgkmcnt(4)
	v_add_f32_e32 v50, v252, v50
	v_add_f32_e32 v51, v253, v51
	s_mov_b32 s43, 0x2d0c00
	buffer_store_dwordx2 v[50:51], v11, s[32:35], s43 offen nt
	s_waitcnt lgkmcnt(3)
	v_add_f32_e32 v52, v252, v52
	v_add_f32_e32 v53, v253, v53
	s_mov_b32 s44, 0x3c1000
	buffer_store_dwordx2 v[52:53], v11, s[32:35], s44 offen nt
	s_waitcnt lgkmcnt(2)
	v_add_f32_e32 v54, v252, v54
	v_add_f32_e32 v55, v253, v55
	s_mov_b32 s45, 0x4b1400
	buffer_store_dwordx2 v[54:55], v11, s[32:35], s45 offen nt
	s_waitcnt lgkmcnt(1)
	v_add_f32_e32 v56, v252, v56
	v_add_f32_e32 v57, v253, v57
	s_mov_b32 s46, 0x5a1800
	buffer_store_dwordx2 v[56:57], v11, s[32:35], s46 offen nt
	s_waitcnt lgkmcnt(0)
	v_add_f32_e32 v58, v252, v58
	v_add_f32_e32 v59, v253, v59
	s_mov_b32 s47, 0x691c00
	buffer_store_dwordx2 v[58:59], v11, s[32:35], s47 offen nt
	ds_read_b64 v[60:61], v12 offset:33792
	ds_read_b64 v[62:63], v12 offset:38016
	ds_read_b64 v[64:65], v12 offset:42240
	ds_read_b64 v[66:67], v12 offset:46464
	ds_read_b64 v[68:69], v12 offset:50688
	ds_read_b64 v[70:71], v12 offset:54912
	ds_read_b64 v[72:73], v12 offset:59136
	ds_read_b64 v[74:75], v12 offset:63360
	s_waitcnt lgkmcnt(7)
	v_add_f32_e32 v60, v252, v60
	v_add_f32_e32 v61, v253, v61
	s_mov_b32 s40, 0x782000
	buffer_store_dwordx2 v[60:61], v11, s[32:35], s40 offen nt
	s_waitcnt lgkmcnt(6)
	v_add_f32_e32 v62, v252, v62
	v_add_f32_e32 v63, v253, v63
	s_mov_b32 s41, 0x872400
	buffer_store_dwordx2 v[62:63], v11, s[32:35], s41 offen nt
	s_waitcnt lgkmcnt(5)
	v_add_f32_e32 v64, v252, v64
	v_add_f32_e32 v65, v253, v65
	s_mov_b32 s42, 0x962800
	buffer_store_dwordx2 v[64:65], v11, s[32:35], s42 offen nt
	s_waitcnt lgkmcnt(4)
	v_add_f32_e32 v66, v252, v66
	v_add_f32_e32 v67, v253, v67
	s_mov_b32 s43, 0xa52c00
	buffer_store_dwordx2 v[66:67], v11, s[32:35], s43 offen nt
	s_waitcnt lgkmcnt(3)
	v_add_f32_e32 v68, v252, v68
	v_add_f32_e32 v69, v253, v69
	s_mov_b32 s44, 0xb43000
	buffer_store_dwordx2 v[68:69], v11, s[32:35], s44 offen nt
	s_waitcnt lgkmcnt(2)
	v_add_f32_e32 v70, v252, v70
	v_add_f32_e32 v71, v253, v71
	s_mov_b32 s45, 0xc33400
	buffer_store_dwordx2 v[70:71], v11, s[32:35], s45 offen nt
	s_waitcnt lgkmcnt(1)
	v_add_f32_e32 v72, v252, v72
	v_add_f32_e32 v73, v253, v73
	s_mov_b32 s46, 0xd23800
	buffer_store_dwordx2 v[72:73], v11, s[32:35], s46 offen nt
	s_waitcnt lgkmcnt(0)
	v_add_f32_e32 v74, v252, v74
	v_add_f32_e32 v75, v253, v75
	s_mov_b32 s47, 0xe13c00
	buffer_store_dwordx2 v[74:75], v11, s[32:35], s47 offen nt
	s_endpgm
